# ret_out (p13): logsigmoid(gamma) computed once per phase into a lane table instead of twice per item
# speedup vs baseline: 1.0083x; 1.0083x over previous
.LBB0_1272:
	s_or_b64 exec, exec, s[4:5]
	s_mov_b32 s0, 0
	v_mov_b32_e32 v70, v0
	s_mov_b64 s[4:5], s[78:79]
	s_waitcnt lgkmcnt(0)
	s_barrier
	s_cmpk_gt_i32 s96, 0x7f
	v_writelane_b32 v232, s0, 41
	s_cselect_b64 s[2:3], -1, 0
	s_nop 0
	v_writelane_b32 v232, s1, 42
	v_readfirstlane_b32 s0, v70
	s_nop 1
	v_writelane_b32 v232, s0, 43
	v_writelane_b32 v232, s2, 44
	s_mov_b64 s[0:1], -1
	s_and_b64 vcc, exec, s[2:3]
	v_writelane_b32 v232, s3, 45
	v_writelane_b32 v232, s90, 46
	s_nop 1
	v_writelane_b32 v232, s91, 47
	v_writelane_b32 v232, s87, 48
	v_writelane_b32 v232, s95, 49
	v_writelane_b32 v232, s96, 51
	s_nop 1
	v_writelane_b32 v232, s97, 52
	s_cbranch_vccz .LBB0_1296
	v_writelane_b32 v232, s62, 53
	s_add_u32 s92, s4, 0x16400000
	v_writelane_b32 v232, s94, 54
	s_addc_u32 s93, s5, 0
	s_add_i32 s2, s96, 0xffffff80
	v_writelane_b32 v232, s95, 55
	s_add_i32 s6, s90, 0xffffff80
	s_mov_b32 s0, s2
	v_writelane_b32 v232, s0, 56
	s_cmpk_gt_u32 s2, 0x3ff
	v_readfirstlane_b32 s8, v70
	v_writelane_b32 v232, s1, 57
	s_cbranch_scc1 .LBB0_1286
	v_readlane_b32 s0, v232, 41
	v_readlane_b32 s1, v232, 42
	s_mov_b32 s2, s0
	s_lshl_b32 s0, s0, 4
	s_ashr_i32 s1, s0, 31
	v_readlane_b32 s12, v233, 0
	s_lshl_b64 s[0:1], s[0:1], 2
	v_readlane_b32 s22, v233, 10
	v_readlane_b32 s23, v233, 11
	s_add_u32 s78, s22, s0
	s_addc_u32 s79, s23, s1
	s_lshl_b32 s0, s2, 9
	s_ashr_i32 s1, s0, 31
	v_readlane_b32 s24, v233, 12
	s_lshl_b64 s[0:1], s[0:1], 2
	v_readlane_b32 s25, v233, 13
	s_add_u32 s0, s24, s0
	s_addc_u32 s1, s25, s1
	s_add_u32 s80, s4, 0x1a400000
	s_addc_u32 s81, s5, 0
	s_add_u32 s7, s4, 0x29400000
	v_readlane_b32 s2, v232, 51
	v_readlane_b32 s84, v232, 56
	s_addc_u32 s77, s5, 0
	s_and_b32 s2, s2, 31
	s_lshr_b32 s9, s84, 8
	s_lshl_b32 s10, s9, 12
	s_lshl_b32 s11, s2, 7
	v_readlane_b32 s3, v232, 52
	s_or_b32 s10, s10, s11
	s_bfe_u32 s3, s84, 0x30005
	s_mulk_i32 s10, 0x3400
	s_add_u32 s10, s80, s10
	s_addc_u32 s11, s81, 0
	s_lshl_b32 s12, s3, 7
	s_add_u32 s10, s10, s12
	s_addc_u32 s11, s11, 0
	s_lshl_b32 s9, s9, 4
	s_lshl_b32 s3, s3, 1
	s_or_b32 s3, s3, s9
	s_lshl_b32 s9, s3, 18
	s_lshl_b32 s12, s2, 13
	s_or_b32 s9, s9, s12
	v_readlane_b32 s13, v233, 1
	s_add_u32 s12, s7, s9
	s_addc_u32 s13, s77, 0
	s_lshl_b32 s3, s3, 5
	s_or_b32 s2, s3, s2
	v_readlane_b32 s14, v233, 2
	v_readlane_b32 s15, v233, 3
	s_mov_b32 s83, 0
	s_or_b32 s82, s2, 32
	s_lshl_b64 s[14:15], s[82:83], 13
	s_waitcnt vmcnt(0)
	v_lshlrev_b32_e32 v1, 3, v70
	v_lshlrev_b32_e32 v29, 2, v70
	v_add_u32_e32 v38, 0x200, v70
	s_add_u32 s14, s7, s14
	v_and_b32_e32 v26, 56, v1
	v_mov_b32_e32 v73, 0
	v_and_b32_e32 v28, 60, v29
	v_and_b32_e32 v16, 0xffffffc0, v29
	v_lshlrev_b32_e32 v36, 2, v38
	s_addc_u32 s15, s77, s15
	v_lshlrev_b32_e32 v72, 1, v26
	v_lshlrev_b32_e32 v30, 1, v28
	v_mov_b32_e32 v31, v73
	v_ashrrev_i32_e32 v17, 31, v16
	v_and_b32_e32 v36, 0xffffffc0, v36
	s_movk_i32 s90, 0x3400
	v_lshl_add_u64 v[14:15], s[10:11], 0, v[72:73]
	v_lshl_add_u64 v[32:33], s[12:13], 0, v[30:31]
	v_lshl_add_u64 v[34:35], s[14:15], 0, v[30:31]
	v_ashrrev_i32_e32 v31, 3, v70
	v_lshlrev_b64 v[76:77], 1, v[16:17]
	v_ashrrev_i32_e32 v37, 31, v36
	v_mad_i64_i32 v[10:11], s[10:11], v31, s90, v[14:15]
	v_lshl_add_u64 v[16:17], v[32:33], 0, v[76:77]
	v_ashrrev_i32_e32 v39, 3, v38
	v_lshlrev_b64 v[80:81], 1, v[36:37]
	global_load_dwordx4 v[2:5], v[10:11], off
	global_load_dwordx4 v[6:9], v[10:11], off offset:1024
	s_nop 0
	global_load_dwordx4 v[10:13], v[10:11], off offset:2048
	v_mad_i64_i32 v[22:23], s[10:11], v39, s90, v[14:15]
	global_load_dwordx2 v[94:95], v[16:17], off
	v_lshl_add_u64 v[16:17], v[34:35], 0, v[76:77]
	v_lshl_add_u64 v[32:33], v[32:33], 0, v[80:81]
	global_load_dwordx2 v[96:97], v[16:17], off
	s_nop 0
	global_load_dwordx4 v[14:17], v[22:23], off
	global_load_dwordx4 v[18:21], v[22:23], off offset:1024
	s_nop 0
	global_load_dwordx4 v[22:25], v[22:23], off offset:2048
	s_ashr_i32 s2, s8, 2
	global_load_dwordx2 v[98:99], v[32:33], off
	v_lshl_add_u64 v[32:33], v[34:35], 0, v[80:81]
	global_load_dwordx2 v[100:101], v[32:33], off
	v_bfi_b32 v82, -16, s2, v70
	s_movk_i32 s2, 0x90
	v_add_u32_e32 v34, 0, v30
	v_mul_lo_u32 v30, v82, s2
	v_add_u32_e32 v33, 0, v30
	v_lshrrev_b32_e32 v30, 2, v70
	v_and_b32_e32 v30, 12, v30
	v_sub_u32_e32 v41, 0x80, v82
	v_add_u32_e32 v32, 0, v72
	s_movk_i32 s3, 0x80
	v_cvt_f32_i32_e32 v71, v41
	v_bfrev_b32_e32 v41, 0.5
	v_lshlrev_b32_e32 v72, 2, v30
	v_mad_i64_i32 v[74:75], s[10:11], v31, s90, 0
	v_and_b32_e32 v35, 48, v70
	v_bitop3_b32 v116, v29, 64, v41 bitop3:0x6c
	v_bitop3_b32 v117, v29, s3, v41 bitop3:0x6c
	v_lshl_add_u64 v[84:85], s[0:1], 0, v[72:73]
	v_mad_u64_u32 v[86:87], s[0:1], v31, s2, v[32:33]
	v_lshrrev_b32_e32 v29, 4, v70
	v_sub_u32_e32 v31, v82, v30
	v_mad_u64_u32 v[88:89], s[0:1], v29, s2, v[34:35]
	v_cvt_f32_i32_e32 v87, v31
	v_sub_u32_e32 v31, v30, v82
	v_lshrrev_b32_e32 v29, 4, v38
	v_cvt_f32_i32_e32 v89, v31
	v_or_b32_e32 v31, 1, v30
	v_mad_u64_u32 v[90:91], s[0:1], v39, s2, v[32:33]
	v_mad_u64_u32 v[92:93], s[0:1], v29, s2, v[34:35]
	v_sub_u32_e32 v32, v31, v82
	v_sub_u32_e32 v31, v82, v31
	v_cvt_f32_i32_e32 v93, v31
	v_or_b32_e32 v31, 2, v30
	v_cvt_f32_i32_e32 v91, v32
	v_cmp_gt_i32_e64 s[12:13], v31, v82
	v_sub_u32_e32 v32, v82, v31
	v_sub_u32_e32 v31, v31, v82
	v_cvt_f32_i32_e32 v119, v31
	v_or_b32_e32 v31, 3, v30
	v_cvt_f32_i32_e32 v118, v32
	v_cmp_gt_i32_e64 s[14:15], v31, v82
	v_sub_u32_e32 v32, v82, v31
	v_sub_u32_e32 v31, v31, v82
	v_readlane_b32 s16, v233, 4
	v_readlane_b32 s17, v233, 5
	v_cvt_f32_i32_e32 v121, v31
	v_or_b32_e32 v31, 16, v30
	v_cvt_f32_i32_e32 v120, v32
	v_cmp_gt_i32_e64 s[16:17], v31, v82
	v_sub_u32_e32 v32, v82, v31
	v_sub_u32_e32 v31, v31, v82
	v_readlane_b32 s18, v233, 6
	v_readlane_b32 s19, v233, 7
	v_cvt_f32_i32_e32 v123, v31
	v_or_b32_e32 v31, 17, v30
	v_cvt_f32_i32_e32 v122, v32
	v_cmp_gt_i32_e64 s[18:19], v31, v82
	v_sub_u32_e32 v32, v82, v31
	v_sub_u32_e32 v31, v31, v82
	v_readlane_b32 s20, v233, 8
	v_readlane_b32 s21, v233, 9
	v_cvt_f32_i32_e32 v125, v31
	v_or_b32_e32 v31, 18, v30
	v_cvt_f32_i32_e32 v124, v32
	v_cmp_gt_i32_e64 s[20:21], v31, v82
	v_sub_u32_e32 v32, v82, v31
	v_sub_u32_e32 v31, v31, v82
	v_cvt_f32_i32_e32 v127, v31
	v_or_b32_e32 v31, 19, v30
	v_cvt_f32_i32_e32 v126, v32
	v_cmp_gt_i32_e64 s[22:23], v31, v82
	v_sub_u32_e32 v32, v82, v31
	v_sub_u32_e32 v31, v31, v82
	v_cvt_f32_i32_e32 v129, v31
	v_or_b32_e32 v31, 32, v30
	v_cvt_f32_i32_e32 v128, v32
	v_sub_u32_e32 v32, v82, v31
	v_cvt_f32_i32_e32 v130, v32
	v_sub_u32_e32 v32, v31, v82
	v_readlane_b32 s26, v233, 14
	v_readlane_b32 s27, v233, 15
	v_cvt_f32_i32_e32 v131, v32
	v_or_b32_e32 v32, 33, v30
	v_cmp_gt_i32_e64 s[26:27], v32, v82
	v_sub_u32_e32 v34, v82, v32
	v_sub_u32_e32 v32, v32, v82
	v_cvt_f32_i32_e32 v133, v32
	v_or_b32_e32 v32, 34, v30
	v_cvt_f32_i32_e32 v132, v34
	v_cmp_gt_i32_e64 s[28:29], v32, v82
	v_sub_u32_e32 v34, v82, v32
	v_sub_u32_e32 v32, v32, v82
	v_cvt_f32_i32_e32 v135, v32
	v_or_b32_e32 v32, 35, v30
	v_cvt_f32_i32_e32 v134, v34
	v_cmp_gt_i32_e64 s[30:31], v32, v82
	v_sub_u32_e32 v34, v82, v32
	v_sub_u32_e32 v32, v32, v82
	v_cvt_f32_i32_e32 v137, v32
	v_or_b32_e32 v32, 48, v30
	v_cvt_f32_i32_e32 v136, v34
	v_cmp_gt_i32_e64 s[34:35], v32, v82
	v_sub_u32_e32 v34, v82, v32
	v_sub_u32_e32 v32, v32, v82
	v_cvt_f32_i32_e32 v139, v32
	v_or_b32_e32 v32, 49, v30
	v_cvt_f32_i32_e32 v138, v34
	v_cmp_gt_i32_e64 s[36:37], v32, v82
	v_sub_u32_e32 v34, v82, v32
	v_sub_u32_e32 v32, v32, v82
	v_cvt_f32_i32_e32 v141, v32
	v_or_b32_e32 v32, 50, v30
	v_cvt_f32_i32_e32 v140, v34
	v_cmp_gt_i32_e64 s[38:39], v32, v82
	v_sub_u32_e32 v34, v82, v32
	v_sub_u32_e32 v32, v32, v82
	v_cvt_f32_i32_e32 v143, v32
	v_or_b32_e32 v32, 51, v30
	v_cvt_f32_i32_e32 v142, v34
	v_cmp_gt_i32_e64 s[40:41], v32, v82
	v_sub_u32_e32 v34, v82, v32
	v_sub_u32_e32 v32, v32, v82
	v_cvt_f32_i32_e32 v145, v32
	v_or_b32_e32 v32, 64, v30
	v_cvt_f32_i32_e32 v144, v34
	v_sub_u32_e32 v34, v82, v32
	v_cvt_f32_i32_e32 v146, v34
	v_sub_u32_e32 v34, v32, v82
	v_cvt_f32_i32_e32 v147, v34
	v_or_b32_e32 v34, 0x41, v30
	v_cmp_gt_i32_e64 s[44:45], v34, v82
	v_sub_u32_e32 v38, v82, v34
	v_sub_u32_e32 v34, v34, v82
	v_cvt_f32_i32_e32 v149, v34
	v_or_b32_e32 v34, 0x42, v30
	v_cvt_f32_i32_e32 v148, v38
	v_cmp_gt_i32_e64 s[46:47], v34, v82
	v_sub_u32_e32 v38, v82, v34
	v_sub_u32_e32 v34, v34, v82
	v_cvt_f32_i32_e32 v151, v34
	v_or_b32_e32 v34, 0x43, v30
	v_cvt_f32_i32_e32 v150, v38
	v_cmp_gt_i32_e64 s[48:49], v34, v82
	v_sub_u32_e32 v38, v82, v34
	v_sub_u32_e32 v34, v34, v82
	v_cvt_f32_i32_e32 v153, v34
	v_or_b32_e32 v34, 0x50, v30
	v_cvt_f32_i32_e32 v152, v38
	v_cmp_gt_i32_e64 s[50:51], v34, v82
	v_sub_u32_e32 v38, v82, v34
	v_sub_u32_e32 v34, v34, v82
	v_cvt_f32_i32_e32 v155, v34
	v_or_b32_e32 v34, 0x51, v30
	v_cvt_f32_i32_e32 v154, v38
	v_cmp_gt_i32_e64 s[52:53], v34, v82
	v_sub_u32_e32 v38, v82, v34
	v_sub_u32_e32 v34, v34, v82
	v_cvt_f32_i32_e32 v157, v34
	v_or_b32_e32 v34, 0x52, v30
	v_cvt_f32_i32_e32 v156, v38
	v_cmp_gt_i32_e64 s[54:55], v34, v82
	v_sub_u32_e32 v38, v82, v34
	v_sub_u32_e32 v34, v34, v82
	v_cvt_f32_i32_e32 v159, v34
	v_or_b32_e32 v34, 0x53, v30
	v_cvt_f32_i32_e32 v158, v38
	v_cmp_gt_i32_e64 s[94:95], v34, v82
	v_sub_u32_e32 v38, v82, v34
	v_sub_u32_e32 v34, v34, v82
	v_cvt_f32_i32_e32 v161, v34
	v_or_b32_e32 v34, 0x60, v30
	v_cvt_f32_i32_e32 v160, v38
	v_sub_u32_e32 v38, v82, v34
	v_cvt_f32_i32_e32 v162, v38
	v_sub_u32_e32 v38, v34, v82
	v_cvt_f32_i32_e32 v163, v38
	v_or_b32_e32 v38, 0x61, v30
	v_mad_i64_i32 v[78:79], s[10:11], v39, s90, 0
	v_cmp_gt_i32_e64 s[60:61], v38, v82
	v_sub_u32_e32 v39, v82, v38
	v_sub_u32_e32 v38, v38, v82
	v_cvt_f32_i32_e32 v165, v38
	v_or_b32_e32 v38, 0x62, v30
	v_cvt_f32_i32_e32 v164, v39
	v_cmp_gt_i32_e64 s[62:63], v38, v82
	v_sub_u32_e32 v39, v82, v38
	v_sub_u32_e32 v38, v38, v82
	v_cvt_f32_i32_e32 v167, v38
	v_or_b32_e32 v38, 0x63, v30
	v_cvt_f32_i32_e32 v166, v39
	v_cmp_gt_i32_e64 s[64:65], v38, v82
	v_sub_u32_e32 v39, v82, v38
	v_sub_u32_e32 v38, v38, v82
	v_cvt_f32_i32_e32 v169, v38
	v_or_b32_e32 v38, 0x70, v30
	v_cvt_f32_i32_e32 v168, v39
	v_cmp_gt_i32_e64 s[66:67], v38, v82
	v_sub_u32_e32 v39, v82, v38
	v_sub_u32_e32 v38, v38, v82
	v_cvt_f32_i32_e32 v171, v38
	v_or_b32_e32 v38, 0x71, v30
	v_cvt_f32_i32_e32 v170, v39
	v_cmp_gt_i32_e64 s[68:69], v38, v82
	v_sub_u32_e32 v39, v82, v38
	v_sub_u32_e32 v38, v38, v82
	v_cvt_f32_i32_e32 v173, v38
	v_or_b32_e32 v38, 0x72, v30
	v_cvt_f32_i32_e32 v172, v39
	v_cmp_gt_i32_e64 s[70:71], v38, v82
	v_sub_u32_e32 v39, v82, v38
	v_sub_u32_e32 v38, v38, v82
	v_and_b32_e32 v1, 24, v1
	v_cvt_f32_i32_e32 v175, v38
	v_or_b32_e32 v38, 0x73, v30
	v_add_u32_e32 v40, 0, v1
	v_add_u32_e32 v1, 1, v82
	v_cvt_f32_i32_e32 v174, v39
	v_cmp_gt_i32_e64 s[72:73], v38, v82
	v_sub_u32_e32 v39, v82, v38
	v_sub_u32_e32 v38, v38, v82
	v_and_b32_e32 v27, 15, v70
	v_bfe_u32 v37, v70, 2, 2
	v_cvt_f32_i32_e32 v1, v1
	v_cvt_f32_i32_e32 v176, v39
	v_cvt_f32_i32_e32 v177, v38
	v_add_u32_e32 v36, 0, v35
	v_mul_u32_u24_e32 v29, 0x90, v27
	v_cmp_gt_i32_e64 s[24:25], v31, v82
	v_cmp_gt_i32_e64 s[42:43], v32, v82
	v_cmp_gt_i32_e64 s[58:59], v34, v82
	v_or_b32_e32 v38, v30, v37
	v_or_b32_e32 v31, v31, v37
	v_or_b32_e32 v32, v32, v37
	v_or_b32_e32 v34, v34, v37
	v_mul_u32_u24_e32 v27, 0x48, v27
	v_mul_u32_u24_e32 v38, 0x90, v38
	v_mul_u32_u24_e32 v31, 0x90, v31
	v_mul_u32_u24_e32 v32, 0x90, v32
	v_mul_u32_u24_e32 v34, 0x90, v34
	v_lshl_add_u32 v178, v27, 1, v36
	v_ashrrev_i32_e32 v83, 31, v82
	v_cmp_gt_i32_e64 s[8:9], v30, v82
	v_cmp_lt_i32_e64 s[10:11], v30, v82
	v_add_u32_e32 v179, 0x900, v178
	v_add_u32_e32 v180, 0x1200, v178
	v_add_u32_e32 v181, 0x1b00, v178
	s_mov_b32 s91, 0xbfb8aa3b
	s_mov_b32 s89, 0x42ce8ed0
	s_mov_b32 s88, 0xc2b17218
	s_mov_b32 s56, 0x7f800000
	s_mov_b32 s76, 0x3f2aaaab
	v_mov_b32_e32 v182, 0x3ecc95a3
	s_mov_b32 s74, 0x3f317218
	s_mov_b32 s75, 0x33800000
	s_mov_b32 s57, 0x3fb8aa3b
	v_lshlrev_b32_e32 v102, 1, v26
	v_lshlrev_b32_e32 v104, 1, v28
	v_add_u32_e32 v183, v33, v35
	v_add_u32_e32 v184, v36, v29
	v_add_u32_e32 v185, v40, v38
	v_add_u32_e32 v186, v40, v31
	v_add_u32_e32 v187, v40, v32
	v_add_u32_e32 v188, v40, v34
	v_lshlrev_b32_e32 v72, 1, v30
	v_mov_b32_e32 v189, 0x3a27c5ac
	v_mov_b32_e32 v190, 0x260
	v_mov_b32_e32 v191, 0x7f800000
	v_mov_b32_e32 v106, 0x3f317218
	s_mov_b32 s82, s84
	v_readlane_b32 s85, v232, 57
	v_mbcnt_lo_u32_b32 v221, -1, 0
	v_mbcnt_hi_u32_b32 v221, -1, v221
	s_mov_b32 s97, 0
.Llsg_ro0_loop:
	s_lshl_b32 s0, s97, 2
	v_mov_b32_e32 v26, s0
	global_load_dword v26, v26, s[78:79]
	s_waitcnt vmcnt(0)
	v_cmp_ngt_f32_e32 vcc, 0, v26
	s_cbranch_vccz .Llsg_ro0_a
	v_mul_f32_e32 v27, 0xbfb8aa3b, v26
	v_rndne_f32_e32 v28, v27
	v_sub_f32_e32 v29, v27, v28
	v_fma_f32 v27, v26, s91, -v27
	v_fmac_f32_e32 v27, 0xb2a5705f, v26
	v_add_f32_e32 v27, v29, v27
	v_cvt_i32_f32_e32 v28, v28
	v_exp_f32_e32 v27, v27
	v_cmp_nlt_f32_e32 vcc, s89, v26
	v_ldexp_f32 v27, v27, v28
	s_nop 0
	v_cndmask_b32_e32 v27, 0, v27, vcc
	v_cmp_ngt_f32_e32 vcc, s88, v26
	s_nop 1
	v_cndmask_b32_e32 v27, v191, v27, vcc
	v_add_f32_e32 v30, 1.0, v27
	v_add_f32_e32 v28, -1.0, v30
	v_sub_f32_e32 v29, v28, v30
	v_add_f32_e32 v29, 1.0, v29
	v_sub_f32_e32 v28, v27, v28
	v_add_f32_e32 v31, v28, v29
	v_frexp_mant_f32_e32 v32, v30
	v_cvt_f64_f32_e32 v[28:29], v30
	v_frexp_exp_i32_f64_e32 v28, v[28:29]
	v_cmp_gt_f32_e32 vcc, s76, v32
	s_nop 1
	v_subbrev_co_u32_e32 v36, vcc, 0, v28, vcc
	v_sub_u32_e32 v28, 0, v36
	v_ldexp_f32 v29, v30, v28
	v_add_f32_e32 v30, -1.0, v29
	v_add_f32_e32 v32, 1.0, v29
	v_ldexp_f32 v28, v31, v28
	v_add_f32_e32 v31, 1.0, v30
	v_add_f32_e32 v33, -1.0, v32
	v_sub_f32_e32 v31, v29, v31
	v_sub_f32_e32 v29, v29, v33
	v_add_f32_e32 v31, v28, v31
	v_add_f32_e32 v28, v28, v29
	v_add_f32_e32 v37, v32, v28
	v_rcp_f32_e32 v39, v37
	v_sub_f32_e32 v29, v32, v37
	v_add_f32_e32 v38, v28, v29
	v_add_f32_e32 v29, v30, v31
	v_mul_f32_e32 v41, v29, v39
	v_sub_f32_e32 v28, v30, v29
	v_mul_f32_e32 v30, v37, v41
	v_fma_f32 v32, v41, v37, -v30
	v_fmac_f32_e32 v32, v41, v38
	v_add_f32_e32 v40, v31, v28
	v_add_f32_e32 v28, v30, v32
	v_sub_f32_e32 v31, v29, v28
	v_pk_add_f32 v[34:35], v[28:29], v[30:31] neg_lo:[0,1] neg_hi:[0,1]
	v_mov_b32_e32 v33, v28
	v_pk_add_f32 v[28:29], v[34:35], v[32:33] neg_lo:[0,1] neg_hi:[0,1]
	v_cmp_neq_f32_e32 vcc, s56, v27
	v_add_f32_e32 v29, v40, v29
	v_add_f32_e32 v28, v28, v29
	v_add_f32_e32 v29, v31, v28
	v_mul_f32_e32 v40, v39, v29
	v_mul_f32_e32 v30, v37, v40
	v_fma_f32 v32, v40, v37, -v30
	v_fmac_f32_e32 v32, v40, v38
	v_sub_f32_e32 v31, v31, v29
	v_add_f32_e32 v37, v28, v31
	v_add_f32_e32 v28, v30, v32
	v_sub_f32_e32 v31, v29, v28
	v_pk_add_f32 v[34:35], v[28:29], v[30:31] neg_lo:[0,1] neg_hi:[0,1]
	v_mov_b32_e32 v33, v28
	v_pk_add_f32 v[28:29], v[34:35], v[32:33] neg_lo:[0,1] neg_hi:[0,1]
	s_nop 0
	v_add_f32_e32 v29, v37, v29
	v_add_f32_e32 v28, v28, v29
	v_add_f32_e32 v29, v41, v40
	v_add_f32_e32 v28, v31, v28
	v_sub_f32_e32 v30, v29, v41
	v_mul_f32_e32 v28, v39, v28
	v_sub_f32_e32 v30, v40, v30
	v_add_f32_e32 v30, v30, v28
	v_add_f32_e32 v32, v29, v30
	v_mul_f32_e32 v33, v32, v32
	v_fmamk_f32 v28, v33, 0x3e9b6dac, v182
	v_fmaak_f32 v107, v33, v28, 0x3f2aaada
	v_cvt_f32_i32_e32 v28, v36
	v_sub_f32_e32 v29, v32, v29
	v_sub_f32_e32 v29, v30, v29
	v_ldexp_f32 v34, v29, 1
	v_mul_f32_e32 v29, v32, v33
	v_ldexp_f32 v31, v32, 1
	v_pk_mul_f32 v[32:33], v[28:29], v[106:107]
	s_nop 0
	v_fma_f32 v30, v28, s74, -v32
	v_fmac_f32_e32 v30, 0xb102e308, v28
	v_pk_add_f32 v[28:29], v[32:33], v[30:31]
	s_nop 0
	v_sub_f32_e32 v31, v29, v31
	v_sub_f32_e32 v31, v33, v31
	v_add_f32_e32 v35, v34, v31
	v_mov_b32_e32 v34, v32
	v_pk_add_f32 v[32:33], v[28:29], v[32:33] neg_lo:[0,1] neg_hi:[0,1]
	v_pk_add_f32 v[36:37], v[28:29], v[34:35]
	v_mov_b32_e32 v31, v28
	v_mov_b32_e32 v33, v37
	v_pk_add_f32 v[38:39], v[30:31], v[32:33] neg_lo:[0,1] neg_hi:[0,1]
	v_pk_add_f32 v[30:31], v[30:31], v[32:33]
	v_mov_b32_e32 v42, v29
	v_pk_add_f32 v[32:33], v[30:31], v[28:29] op_sel:[1,0] op_sel_hi:[0,1] neg_lo:[0,1] neg_hi:[0,1]
	v_pk_add_f32 v[40:41], v[36:37], v[32:33] op_sel_hi:[1,0] neg_lo:[0,1] neg_hi:[0,1]
	v_mov_b32_e32 v36, v37
	v_mov_b32_e32 v37, v31
	v_mov_b32_e32 v43, v32
	v_pk_add_f32 v[32:33], v[36:37], v[42:43] neg_lo:[0,1] neg_hi:[0,1]
	v_mov_b32_e32 v34, v35
	v_mov_b32_e32 v35, v28
	v_pk_add_f32 v[28:29], v[34:35], v[32:33] neg_lo:[0,1] neg_hi:[0,1]
	v_mov_b32_e32 v40, v38
	v_pk_add_f32 v[32:33], v[40:41], v[28:29]
	v_mov_b32_e32 v39, v31
	v_pk_add_f32 v[34:35], v[32:33], v[32:33] op_sel:[0,1] op_sel_hi:[1,0]
	s_nop 0
	v_pk_add_f32 v[30:31], v[30:31], v[34:35] op_sel:[1,0] op_sel_hi:[0,1]
	v_mov_b32_e32 v33, v30
	v_pk_add_f32 v[36:37], v[32:33], v[38:39] neg_lo:[0,1] neg_hi:[0,1]
	v_mov_b32_e32 v29, v34
	v_sub_f32_e32 v31, v32, v36
	v_pk_add_f32 v[28:29], v[28:29], v[36:37] neg_lo:[0,1] neg_hi:[0,1]
	v_sub_f32_e32 v31, v38, v31
	v_add_f32_e32 v28, v28, v31
	v_add_f32_e32 v28, v28, v29
	v_add_f32_e32 v28, v30, v28
	v_cndmask_b32_e32 v28, v191, v28, vcc
	v_cmp_lt_f32_e64 vcc, |v27|, s75
	s_nop 1
	v_cndmask_b32_e32 v27, v28, v27, vcc
	v_xor_b32_e32 v108, 0x80000000, v27
	s_cbranch_execz .Llsg_ro0_b
	s_branch .Llsg_ro0_c

.Llsg_ro0_c:
	s_nop 0
	v_cmp_eq_u32_e32 vcc, s97, v221
	s_nop 1
	v_cndmask_b32_e32 v222, v222, v108, vcc
	s_add_i32 s97, s97, 1
	s_cmp_lt_u32 s97, 16
	s_cbranch_scc1 .Llsg_ro0_loop
	s_branch .LBB0_1276

.LBB0_1276:
	s_ashr_i32 s86, s82, 31
	s_lshr_b32 s0, s86, 27
	s_add_i32 s0, s82, s0
	s_ashr_i32 s87, s0, 5
	s_and_b32 s97, s87, 7
	s_lshl_b32 s0, s97, 2
	v_mov_b32_e32 v26, s0
	s_add_u32 s0, s78, s0
	s_addc_u32 s1, s79, 0
	s_waitcnt vmcnt(0)
	v_readlane_b32 s2, v222, s97
	s_nop 1
	v_mov_b32_e32 v108, s2
	s_add_i32 s2, s97, 8
	s_nop 0
	v_readlane_b32 s2, v222, s2
	s_nop 1
	v_mov_b32_e32 v107, s2

.LBB0_3590:
	s_or_b64 exec, exec, s[4:5]
	s_mov_b32 s0, 1
	s_mov_b64 s[4:5], s[74:75]
	v_mov_b32_e32 v70, v0
	s_waitcnt lgkmcnt(0)
	s_barrier
	s_nop 0
	v_writelane_b32 v232, s0, 49
	v_readfirstlane_b32 s8, v70
	s_nop 0
	v_writelane_b32 v232, s1, 50
	s_mov_b64 s[0:1], -1
	v_readlane_b32 s2, v232, 44
	v_readlane_b32 s3, v232, 45
	s_and_b64 vcc, exec, s[2:3]
	s_cbranch_vccz .LBB0_3614
	v_writelane_b32 v232, s8, 25
	v_writelane_b32 v232, s60, 24
	v_writelane_b32 v232, s93, 23
	s_add_u32 s80, s4, 0x16400000
	v_writelane_b32 v232, s94, 54
	s_addc_u32 s81, s5, 0
	s_add_i32 s2, s96, 0xffffff80
	v_writelane_b32 v232, s95, 55
	s_add_i32 s90, s76, 0xffffff80
	s_mov_b32 s0, s2
	v_writelane_b32 v232, s0, 21
	s_cmpk_gt_u32 s2, 0x3ff
	v_readfirstlane_b32 s6, v70
	v_writelane_b32 v232, s1, 22
	s_cbranch_scc1 .LBB0_3604
	v_readlane_b32 s0, v232, 49
	v_readlane_b32 s1, v232, 50
	s_mov_b32 s2, s0
	s_lshl_b32 s0, s0, 4
	s_ashr_i32 s1, s0, 31
	v_readlane_b32 s8, v233, 0
	s_lshl_b64 s[0:1], s[0:1], 2
	v_readlane_b32 s18, v233, 10
	v_readlane_b32 s19, v233, 11
	s_add_u32 s82, s18, s0
	s_addc_u32 s83, s19, s1
	s_lshl_b32 s0, s2, 9
	s_ashr_i32 s1, s0, 31
	v_readlane_b32 s20, v233, 12
	s_lshl_b64 s[0:1], s[0:1], 2
	v_readlane_b32 s21, v233, 13
	s_add_u32 s0, s20, s0
	s_addc_u32 s1, s21, s1
	s_add_u32 s84, s4, 0x1a400000
	s_addc_u32 s85, s5, 0
	v_readlane_b32 s9, v233, 1
	s_add_u32 s77, s4, 0x29400000
	v_readlane_b32 s2, v232, 51
	v_readlane_b32 s88, v232, 21
	s_addc_u32 s91, s5, 0
	v_readlane_b32 s3, v232, 52
	s_and_b32 s7, s2, 31
	s_lshr_b32 s9, s88, 8
	s_lshl_b32 s2, s9, 12
	s_lshl_b32 s3, s7, 7
	s_or_b32 s2, s2, s3
	s_bfe_u32 s8, s88, 0x30005
	s_mulk_i32 s2, 0x3400
	v_readlane_b32 s10, v233, 2
	s_add_u32 s2, s84, s2
	s_addc_u32 s3, s85, 0
	s_lshl_b32 s10, s8, 7
	s_add_u32 s2, s2, s10
	s_addc_u32 s3, s3, 0
	s_lshl_b32 s9, s9, 4
	s_lshl_b32 s8, s8, 1
	s_or_b32 s10, s8, s9
	s_lshl_b32 s8, s10, 18
	s_lshl_b32 s9, s7, 13
	s_or_b32 s8, s8, s9
	s_add_u32 s8, s77, s8
	s_addc_u32 s9, s91, 0
	s_lshl_b32 s10, s10, 5
	s_or_b32 s7, s10, s7
	v_readlane_b32 s11, v233, 3
	s_mov_b32 s87, 0
	s_or_b32 s86, s7, 32
	s_lshl_b64 s[10:11], s[86:87], 13
	s_waitcnt vmcnt(0)
	v_lshlrev_b32_e32 v1, 3, v70
	v_lshlrev_b32_e32 v29, 2, v70
	v_add_u32_e32 v38, 0x200, v70
	s_add_u32 s10, s77, s10
	v_and_b32_e32 v26, 56, v1
	v_mov_b32_e32 v73, 0
	v_and_b32_e32 v28, 60, v29
	v_and_b32_e32 v16, 0xffffffc0, v29
	v_lshlrev_b32_e32 v36, 2, v38
	s_addc_u32 s11, s91, s11
	v_lshlrev_b32_e32 v72, 1, v26
	v_lshlrev_b32_e32 v30, 1, v28
	v_mov_b32_e32 v31, v73
	v_ashrrev_i32_e32 v17, 31, v16
	v_and_b32_e32 v36, 0xffffffc0, v36
	s_movk_i32 s95, 0x3400
	v_lshl_add_u64 v[14:15], s[2:3], 0, v[72:73]
	v_lshl_add_u64 v[32:33], s[8:9], 0, v[30:31]
	v_lshl_add_u64 v[34:35], s[10:11], 0, v[30:31]
	v_ashrrev_i32_e32 v31, 3, v70
	v_lshlrev_b64 v[76:77], 1, v[16:17]
	v_ashrrev_i32_e32 v37, 31, v36
	v_mad_i64_i32 v[10:11], s[2:3], v31, s95, v[14:15]
	v_lshl_add_u64 v[16:17], v[32:33], 0, v[76:77]
	v_ashrrev_i32_e32 v39, 3, v38
	v_lshlrev_b64 v[80:81], 1, v[36:37]
	global_load_dwordx4 v[2:5], v[10:11], off
	global_load_dwordx4 v[6:9], v[10:11], off offset:1024
	s_nop 0
	global_load_dwordx4 v[10:13], v[10:11], off offset:2048
	v_mad_i64_i32 v[22:23], s[2:3], v39, s95, v[14:15]
	global_load_dwordx2 v[94:95], v[16:17], off
	v_lshl_add_u64 v[16:17], v[34:35], 0, v[76:77]
	v_lshl_add_u64 v[32:33], v[32:33], 0, v[80:81]
	global_load_dwordx2 v[96:97], v[16:17], off
	s_nop 0
	global_load_dwordx4 v[14:17], v[22:23], off
	global_load_dwordx4 v[18:21], v[22:23], off offset:1024
	s_nop 0
	global_load_dwordx4 v[22:25], v[22:23], off offset:2048
	v_mad_i64_i32 v[74:75], s[2:3], v31, s95, 0
	global_load_dwordx2 v[98:99], v[32:33], off
	v_lshl_add_u64 v[32:33], v[34:35], 0, v[80:81]
	global_load_dwordx2 v[100:101], v[32:33], off
	v_mad_i64_i32 v[78:79], s[2:3], v39, s95, 0
	s_ashr_i32 s2, s6, 2
	s_nop 0
	v_bfi_b32 v82, -16, s2, v70
	s_movk_i32 s2, 0x90
	v_add_u32_e32 v34, 0, v30
	v_mul_lo_u32 v30, v82, s2
	v_add_u32_e32 v33, 0, v30
	v_lshrrev_b32_e32 v30, 2, v70
	v_and_b32_e32 v30, 12, v30
	v_sub_u32_e32 v41, 0x80, v82
	v_add_u32_e32 v32, 0, v72
	s_movk_i32 s3, 0x80
	v_cvt_f32_i32_e32 v71, v41
	v_bfrev_b32_e32 v41, 0.5
	v_lshlrev_b32_e32 v72, 2, v30
	v_and_b32_e32 v35, 48, v70
	v_bitop3_b32 v116, v29, 64, v41 bitop3:0x6c
	v_bitop3_b32 v117, v29, s3, v41 bitop3:0x6c
	v_lshl_add_u64 v[84:85], s[0:1], 0, v[72:73]
	v_mad_u64_u32 v[86:87], s[0:1], v31, s2, v[32:33]
	v_lshrrev_b32_e32 v29, 4, v70
	v_sub_u32_e32 v31, v82, v30
	v_mad_u64_u32 v[88:89], s[0:1], v29, s2, v[34:35]
	v_cvt_f32_i32_e32 v87, v31
	v_sub_u32_e32 v31, v30, v82
	v_lshrrev_b32_e32 v29, 4, v38
	v_cvt_f32_i32_e32 v89, v31
	v_or_b32_e32 v31, 1, v30
	v_mad_u64_u32 v[90:91], s[0:1], v39, s2, v[32:33]
	v_mad_u64_u32 v[92:93], s[0:1], v29, s2, v[34:35]
	v_sub_u32_e32 v32, v31, v82
	v_sub_u32_e32 v31, v82, v31
	v_readlane_b32 s14, v233, 6
	v_readlane_b32 s15, v233, 7
	v_cvt_f32_i32_e32 v93, v31
	v_or_b32_e32 v31, 2, v30
	v_cvt_f32_i32_e32 v91, v32
	v_cmp_gt_i32_e64 s[14:15], v31, v82
	v_sub_u32_e32 v32, v82, v31
	v_sub_u32_e32 v31, v31, v82
	v_readlane_b32 s16, v233, 8
	v_readlane_b32 s17, v233, 9
	v_cvt_f32_i32_e32 v119, v31
	v_or_b32_e32 v31, 3, v30
	v_cvt_f32_i32_e32 v118, v32
	v_cmp_gt_i32_e64 s[16:17], v31, v82
	v_sub_u32_e32 v32, v82, v31
	v_sub_u32_e32 v31, v31, v82
	v_cvt_f32_i32_e32 v121, v31
	v_or_b32_e32 v31, 16, v30
	v_cvt_f32_i32_e32 v120, v32
	v_cmp_gt_i32_e64 s[18:19], v31, v82
	v_sub_u32_e32 v32, v82, v31
	v_sub_u32_e32 v31, v31, v82
	v_cvt_f32_i32_e32 v123, v31
	v_or_b32_e32 v31, 17, v30
	v_cvt_f32_i32_e32 v122, v32
	v_cmp_gt_i32_e64 s[20:21], v31, v82
	v_sub_u32_e32 v32, v82, v31
	v_sub_u32_e32 v31, v31, v82
	v_readlane_b32 s22, v233, 14
	v_readlane_b32 s23, v233, 15
	v_cvt_f32_i32_e32 v125, v31
	v_or_b32_e32 v31, 18, v30
	v_cvt_f32_i32_e32 v124, v32
	v_cmp_gt_i32_e64 s[22:23], v31, v82
	v_sub_u32_e32 v32, v82, v31
	v_sub_u32_e32 v31, v31, v82
	v_cvt_f32_i32_e32 v127, v31
	v_or_b32_e32 v31, 19, v30
	v_cvt_f32_i32_e32 v126, v32
	v_cmp_gt_i32_e64 s[24:25], v31, v82
	v_sub_u32_e32 v32, v82, v31
	v_sub_u32_e32 v31, v31, v82
	v_cvt_f32_i32_e32 v129, v31
	v_or_b32_e32 v31, 32, v30
	v_cvt_f32_i32_e32 v128, v32
	v_sub_u32_e32 v32, v82, v31
	v_cvt_f32_i32_e32 v130, v32
	v_sub_u32_e32 v32, v31, v82
	v_cvt_f32_i32_e32 v131, v32
	v_or_b32_e32 v32, 33, v30
	v_cmp_gt_i32_e64 s[28:29], v32, v82
	v_sub_u32_e32 v34, v82, v32
	v_sub_u32_e32 v32, v32, v82
	v_cvt_f32_i32_e32 v133, v32
	v_or_b32_e32 v32, 34, v30
	v_cvt_f32_i32_e32 v132, v34
	v_cmp_gt_i32_e64 s[30:31], v32, v82
	v_sub_u32_e32 v34, v82, v32
	v_sub_u32_e32 v32, v32, v82
	v_cvt_f32_i32_e32 v135, v32
	v_or_b32_e32 v32, 35, v30
	v_cvt_f32_i32_e32 v134, v34
	v_cmp_gt_i32_e64 s[34:35], v32, v82
	v_sub_u32_e32 v34, v82, v32
	v_sub_u32_e32 v32, v32, v82
	v_cvt_f32_i32_e32 v137, v32
	v_or_b32_e32 v32, 48, v30
	v_cvt_f32_i32_e32 v136, v34
	v_cmp_gt_i32_e64 s[36:37], v32, v82
	v_sub_u32_e32 v34, v82, v32
	v_sub_u32_e32 v32, v32, v82
	v_cvt_f32_i32_e32 v139, v32
	v_or_b32_e32 v32, 49, v30
	v_cvt_f32_i32_e32 v138, v34
	v_cmp_gt_i32_e64 s[38:39], v32, v82
	v_sub_u32_e32 v34, v82, v32
	v_sub_u32_e32 v32, v32, v82
	v_cvt_f32_i32_e32 v141, v32
	v_or_b32_e32 v32, 50, v30
	v_cvt_f32_i32_e32 v140, v34
	v_cmp_gt_i32_e64 s[40:41], v32, v82
	v_sub_u32_e32 v34, v82, v32
	v_sub_u32_e32 v32, v32, v82
	v_cvt_f32_i32_e32 v143, v32
	v_or_b32_e32 v32, 51, v30
	v_cvt_f32_i32_e32 v142, v34
	v_cmp_gt_i32_e64 s[42:43], v32, v82
	v_sub_u32_e32 v34, v82, v32
	v_sub_u32_e32 v32, v32, v82
	v_cvt_f32_i32_e32 v145, v32
	v_or_b32_e32 v32, 64, v30
	v_cvt_f32_i32_e32 v144, v34
	v_sub_u32_e32 v34, v82, v32
	v_cvt_f32_i32_e32 v146, v34
	v_sub_u32_e32 v34, v32, v82
	v_cvt_f32_i32_e32 v147, v34
	v_or_b32_e32 v34, 0x41, v30
	v_cmp_gt_i32_e64 s[46:47], v34, v82
	v_sub_u32_e32 v38, v82, v34
	v_sub_u32_e32 v34, v34, v82
	v_cvt_f32_i32_e32 v149, v34
	v_or_b32_e32 v34, 0x42, v30
	v_cvt_f32_i32_e32 v148, v38
	v_cmp_gt_i32_e64 s[48:49], v34, v82
	v_sub_u32_e32 v38, v82, v34
	v_sub_u32_e32 v34, v34, v82
	v_cvt_f32_i32_e32 v151, v34
	v_or_b32_e32 v34, 0x43, v30
	v_cvt_f32_i32_e32 v150, v38
	v_cmp_gt_i32_e64 s[50:51], v34, v82
	v_sub_u32_e32 v38, v82, v34
	v_sub_u32_e32 v34, v34, v82
	v_cvt_f32_i32_e32 v153, v34
	v_or_b32_e32 v34, 0x50, v30
	v_cvt_f32_i32_e32 v152, v38
	v_cmp_gt_i32_e64 s[52:53], v34, v82
	v_sub_u32_e32 v38, v82, v34
	v_sub_u32_e32 v34, v34, v82
	v_cvt_f32_i32_e32 v155, v34
	v_or_b32_e32 v34, 0x51, v30
	v_cvt_f32_i32_e32 v154, v38
	v_cmp_gt_i32_e64 s[54:55], v34, v82
	v_sub_u32_e32 v38, v82, v34
	v_sub_u32_e32 v34, v34, v82
	v_cvt_f32_i32_e32 v157, v34
	v_or_b32_e32 v34, 0x52, v30
	v_cvt_f32_i32_e32 v156, v38
	v_cmp_gt_i32_e64 s[56:57], v34, v82
	v_sub_u32_e32 v38, v82, v34
	v_sub_u32_e32 v34, v34, v82
	v_cvt_f32_i32_e32 v159, v34
	v_or_b32_e32 v34, 0x53, v30
	v_cvt_f32_i32_e32 v158, v38
	v_cmp_gt_i32_e64 s[58:59], v34, v82
	v_sub_u32_e32 v38, v82, v34
	v_sub_u32_e32 v34, v34, v82
	v_cvt_f32_i32_e32 v161, v34
	v_or_b32_e32 v34, 0x60, v30
	v_cvt_f32_i32_e32 v160, v38
	v_sub_u32_e32 v38, v82, v34
	v_cvt_f32_i32_e32 v162, v38
	v_sub_u32_e32 v38, v34, v82
	v_cvt_f32_i32_e32 v163, v38
	v_or_b32_e32 v38, 0x61, v30
	v_cmp_gt_i32_e64 s[62:63], v38, v82
	v_sub_u32_e32 v39, v82, v38
	v_sub_u32_e32 v38, v38, v82
	v_cvt_f32_i32_e32 v165, v38
	v_or_b32_e32 v38, 0x62, v30
	v_cvt_f32_i32_e32 v164, v39
	v_cmp_gt_i32_e64 s[64:65], v38, v82
	v_sub_u32_e32 v39, v82, v38
	v_sub_u32_e32 v38, v38, v82
	v_cvt_f32_i32_e32 v167, v38
	v_or_b32_e32 v38, 0x63, v30
	v_cvt_f32_i32_e32 v166, v39
	v_cmp_gt_i32_e64 s[66:67], v38, v82
	v_sub_u32_e32 v39, v82, v38
	v_sub_u32_e32 v38, v38, v82
	v_cvt_f32_i32_e32 v169, v38
	v_or_b32_e32 v38, 0x70, v30
	v_cvt_f32_i32_e32 v168, v39
	v_cmp_gt_i32_e64 s[68:69], v38, v82
	v_sub_u32_e32 v39, v82, v38
	v_sub_u32_e32 v38, v38, v82
	v_cvt_f32_i32_e32 v171, v38
	v_or_b32_e32 v38, 0x71, v30
	v_cvt_f32_i32_e32 v170, v39
	v_cmp_gt_i32_e64 s[70:71], v38, v82
	v_sub_u32_e32 v39, v82, v38
	v_sub_u32_e32 v38, v38, v82
	v_cvt_f32_i32_e32 v173, v38
	v_or_b32_e32 v38, 0x72, v30
	v_cvt_f32_i32_e32 v172, v39
	v_cmp_gt_i32_e64 s[72:73], v38, v82
	v_sub_u32_e32 v39, v82, v38
	v_sub_u32_e32 v38, v38, v82
	v_and_b32_e32 v1, 24, v1
	v_cvt_f32_i32_e32 v175, v38
	v_or_b32_e32 v38, 0x73, v30
	v_add_u32_e32 v40, 0, v1
	v_add_u32_e32 v1, 1, v82
	v_cvt_f32_i32_e32 v174, v39
	v_cmp_gt_i32_e64 s[74:75], v38, v82
	v_sub_u32_e32 v39, v82, v38
	v_sub_u32_e32 v38, v38, v82
	v_and_b32_e32 v27, 15, v70
	v_bfe_u32 v37, v70, 2, 2
	v_cvt_f32_i32_e32 v1, v1
	v_cvt_f32_i32_e32 v176, v39
	v_cvt_f32_i32_e32 v177, v38
	v_add_u32_e32 v36, 0, v35
	v_mul_u32_u24_e32 v29, 0x90, v27
	v_cmp_gt_i32_e64 s[26:27], v31, v82
	v_cmp_gt_i32_e64 s[44:45], v32, v82
	v_cmp_gt_i32_e64 s[60:61], v34, v82
	v_or_b32_e32 v38, v30, v37
	v_or_b32_e32 v31, v31, v37
	v_or_b32_e32 v32, v32, v37
	v_or_b32_e32 v34, v34, v37
	v_mul_u32_u24_e32 v27, 0x48, v27
	v_readlane_b32 s12, v233, 4
	v_readlane_b32 s13, v233, 5
	v_mul_u32_u24_e32 v38, 0x90, v38
	v_mul_u32_u24_e32 v31, 0x90, v31
	v_mul_u32_u24_e32 v32, 0x90, v32
	v_mul_u32_u24_e32 v34, 0x90, v34
	v_lshl_add_u32 v178, v27, 1, v36
	v_ashrrev_i32_e32 v83, 31, v82
	v_cmp_gt_i32_e64 s[6:7], v30, v82
	v_cmp_lt_i32_e64 s[12:13], v30, v82
	v_add_u32_e32 v179, 0x900, v178
	v_add_u32_e32 v180, 0x1200, v178
	v_add_u32_e32 v181, 0x1b00, v178
	s_mov_b32 s8, 0xbfb8aa3b
	s_mov_b32 s9, 0x42ce8ed0
	s_mov_b32 s10, 0xc2b17218
	s_mov_b32 s94, 0x7f800000
	s_mov_b32 s78, 0x3f2aaaab
	v_mov_b32_e32 v182, 0x3ecc95a3
	s_mov_b32 s11, 0x3f317218
	s_mov_b32 s76, 0x33800000
	s_mov_b32 s79, 0x3fb8aa3b
	v_lshlrev_b32_e32 v102, 1, v26
	v_lshlrev_b32_e32 v104, 1, v28
	v_add_u32_e32 v183, v33, v35
	v_add_u32_e32 v184, v36, v29
	v_add_u32_e32 v185, v40, v38
	v_add_u32_e32 v186, v40, v31
	v_add_u32_e32 v187, v40, v32
	v_add_u32_e32 v188, v40, v34
	v_lshlrev_b32_e32 v72, 1, v30
	v_mov_b32_e32 v189, 0x3a27c5ac
	v_mov_b32_e32 v190, 0x260
	v_mov_b32_e32 v191, 0x7f800000
	v_mov_b32_e32 v106, 0x3f317218
	s_mov_b32 s86, s88
	v_readlane_b32 s89, v232, 22
	v_mbcnt_lo_u32_b32 v221, -1, 0
	v_mbcnt_hi_u32_b32 v221, -1, v221
	s_mov_b32 s97, 0
.Llsg_ro1_loop:
	s_lshl_b32 s0, s97, 2
	v_mov_b32_e32 v26, s0
	global_load_dword v26, v26, s[82:83]
	s_waitcnt vmcnt(0)
	v_cmp_ngt_f32_e32 vcc, 0, v26
	s_cbranch_vccz .Llsg_ro1_a
	v_mul_f32_e32 v27, 0xbfb8aa3b, v26
	v_rndne_f32_e32 v28, v27
	v_sub_f32_e32 v29, v27, v28
	v_fma_f32 v27, v26, s8, -v27
	v_fmac_f32_e32 v27, 0xb2a5705f, v26
	v_add_f32_e32 v27, v29, v27
	v_cvt_i32_f32_e32 v28, v28
	v_exp_f32_e32 v27, v27
	v_cmp_nlt_f32_e32 vcc, s9, v26
	v_ldexp_f32 v27, v27, v28
	s_nop 0
	v_cndmask_b32_e32 v27, 0, v27, vcc
	v_cmp_ngt_f32_e32 vcc, s10, v26
	s_nop 1
	v_cndmask_b32_e32 v27, v191, v27, vcc
	v_add_f32_e32 v30, 1.0, v27
	v_add_f32_e32 v28, -1.0, v30
	v_sub_f32_e32 v29, v28, v30
	v_add_f32_e32 v29, 1.0, v29
	v_sub_f32_e32 v28, v27, v28
	v_add_f32_e32 v31, v28, v29
	v_frexp_mant_f32_e32 v32, v30
	v_cvt_f64_f32_e32 v[28:29], v30
	v_frexp_exp_i32_f64_e32 v28, v[28:29]
	v_cmp_gt_f32_e32 vcc, s78, v32
	s_nop 1
	v_subbrev_co_u32_e32 v36, vcc, 0, v28, vcc
	v_sub_u32_e32 v28, 0, v36
	v_ldexp_f32 v29, v30, v28
	v_add_f32_e32 v30, -1.0, v29
	v_add_f32_e32 v32, 1.0, v29
	v_ldexp_f32 v28, v31, v28
	v_add_f32_e32 v31, 1.0, v30
	v_add_f32_e32 v33, -1.0, v32
	v_sub_f32_e32 v31, v29, v31
	v_sub_f32_e32 v29, v29, v33
	v_add_f32_e32 v31, v28, v31
	v_add_f32_e32 v28, v28, v29
	v_add_f32_e32 v37, v32, v28
	v_rcp_f32_e32 v39, v37
	v_sub_f32_e32 v29, v32, v37
	v_add_f32_e32 v38, v28, v29
	v_add_f32_e32 v29, v30, v31
	v_mul_f32_e32 v41, v29, v39
	v_sub_f32_e32 v28, v30, v29
	v_mul_f32_e32 v30, v37, v41
	v_fma_f32 v32, v41, v37, -v30
	v_fmac_f32_e32 v32, v41, v38
	v_add_f32_e32 v40, v31, v28
	v_add_f32_e32 v28, v30, v32
	v_sub_f32_e32 v31, v29, v28
	v_pk_add_f32 v[34:35], v[28:29], v[30:31] neg_lo:[0,1] neg_hi:[0,1]
	v_mov_b32_e32 v33, v28
	v_pk_add_f32 v[28:29], v[34:35], v[32:33] neg_lo:[0,1] neg_hi:[0,1]
	v_cmp_neq_f32_e32 vcc, s94, v27
	v_add_f32_e32 v29, v40, v29
	v_add_f32_e32 v28, v28, v29
	v_add_f32_e32 v29, v31, v28
	v_mul_f32_e32 v40, v39, v29
	v_mul_f32_e32 v30, v37, v40
	v_fma_f32 v32, v40, v37, -v30
	v_fmac_f32_e32 v32, v40, v38
	v_sub_f32_e32 v31, v31, v29
	v_add_f32_e32 v37, v28, v31
	v_add_f32_e32 v28, v30, v32
	v_sub_f32_e32 v31, v29, v28
	v_pk_add_f32 v[34:35], v[28:29], v[30:31] neg_lo:[0,1] neg_hi:[0,1]
	v_mov_b32_e32 v33, v28
	v_pk_add_f32 v[28:29], v[34:35], v[32:33] neg_lo:[0,1] neg_hi:[0,1]
	s_nop 0
	v_add_f32_e32 v29, v37, v29
	v_add_f32_e32 v28, v28, v29
	v_add_f32_e32 v29, v41, v40
	v_add_f32_e32 v28, v31, v28
	v_sub_f32_e32 v30, v29, v41
	v_mul_f32_e32 v28, v39, v28
	v_sub_f32_e32 v30, v40, v30
	v_add_f32_e32 v30, v30, v28
	v_add_f32_e32 v32, v29, v30
	v_mul_f32_e32 v33, v32, v32
	v_fmamk_f32 v28, v33, 0x3e9b6dac, v182
	v_fmaak_f32 v107, v33, v28, 0x3f2aaada
	v_cvt_f32_i32_e32 v28, v36
	v_sub_f32_e32 v29, v32, v29
	v_sub_f32_e32 v29, v30, v29
	v_ldexp_f32 v34, v29, 1
	v_mul_f32_e32 v29, v32, v33
	v_ldexp_f32 v31, v32, 1
	v_pk_mul_f32 v[32:33], v[28:29], v[106:107]
	s_nop 0
	v_fma_f32 v30, v28, s11, -v32
	v_fmac_f32_e32 v30, 0xb102e308, v28
	v_pk_add_f32 v[28:29], v[32:33], v[30:31]
	s_nop 0
	v_sub_f32_e32 v31, v29, v31
	v_sub_f32_e32 v31, v33, v31
	v_add_f32_e32 v35, v34, v31
	v_mov_b32_e32 v34, v32
	v_pk_add_f32 v[32:33], v[28:29], v[32:33] neg_lo:[0,1] neg_hi:[0,1]
	v_pk_add_f32 v[36:37], v[28:29], v[34:35]
	v_mov_b32_e32 v31, v28
	v_mov_b32_e32 v33, v37
	v_pk_add_f32 v[38:39], v[30:31], v[32:33] neg_lo:[0,1] neg_hi:[0,1]
	v_pk_add_f32 v[30:31], v[30:31], v[32:33]
	v_mov_b32_e32 v42, v29
	v_pk_add_f32 v[32:33], v[30:31], v[28:29] op_sel:[1,0] op_sel_hi:[0,1] neg_lo:[0,1] neg_hi:[0,1]
	v_pk_add_f32 v[40:41], v[36:37], v[32:33] op_sel_hi:[1,0] neg_lo:[0,1] neg_hi:[0,1]
	v_mov_b32_e32 v36, v37
	v_mov_b32_e32 v37, v31
	v_mov_b32_e32 v43, v32
	v_pk_add_f32 v[32:33], v[36:37], v[42:43] neg_lo:[0,1] neg_hi:[0,1]
	v_mov_b32_e32 v34, v35
	v_mov_b32_e32 v35, v28
	v_pk_add_f32 v[28:29], v[34:35], v[32:33] neg_lo:[0,1] neg_hi:[0,1]
	v_mov_b32_e32 v40, v38
	v_pk_add_f32 v[32:33], v[40:41], v[28:29]
	v_mov_b32_e32 v39, v31
	v_pk_add_f32 v[34:35], v[32:33], v[32:33] op_sel:[0,1] op_sel_hi:[1,0]
	s_nop 0
	v_pk_add_f32 v[30:31], v[30:31], v[34:35] op_sel:[1,0] op_sel_hi:[0,1]
	v_mov_b32_e32 v33, v30
	v_pk_add_f32 v[36:37], v[32:33], v[38:39] neg_lo:[0,1] neg_hi:[0,1]
	v_mov_b32_e32 v29, v34
	v_sub_f32_e32 v31, v32, v36
	v_pk_add_f32 v[28:29], v[28:29], v[36:37] neg_lo:[0,1] neg_hi:[0,1]
	v_sub_f32_e32 v31, v38, v31
	v_add_f32_e32 v28, v28, v31
	v_add_f32_e32 v28, v28, v29
	v_add_f32_e32 v28, v30, v28
	v_cndmask_b32_e32 v28, v191, v28, vcc
	v_cmp_lt_f32_e64 vcc, |v27|, s76
	s_nop 1
	v_cndmask_b32_e32 v27, v28, v27, vcc
	v_xor_b32_e32 v108, 0x80000000, v27
	s_cbranch_execz .Llsg_ro1_b
	s_branch .Llsg_ro1_c

.LBB0_3594:
	s_ashr_i32 s92, s86, 31
	s_lshr_b32 s0, s92, 27
	s_add_i32 s0, s86, s0
	s_ashr_i32 s93, s0, 5
	s_and_b32 s97, s93, 7
	s_lshl_b32 s0, s97, 2
	v_mov_b32_e32 v26, s0
	s_add_u32 s0, s82, s0
	s_addc_u32 s1, s83, 0
	s_waitcnt vmcnt(0)
	v_readlane_b32 s2, v222, s97
	s_nop 1
	v_mov_b32_e32 v108, s2
	s_add_i32 s2, s97, 8
	s_nop 0
	v_readlane_b32 s2, v222, s2
	s_nop 1
	v_mov_b32_e32 v107, s2
